# gate fast log-sigmoid + fp6 loop: contiguous operand tuples, VALU-MFMA pads dropped
# baseline (speedup 1.0000x reference)
.LBB0_1257:
	ds_read_b128 v[2:5], v202
	ds_read_b128 v[6:9], v202 offset:1024
	ds_read_b128 v[10:13], v202 offset:2048
	ds_read_b128 v[14:17], v202 offset:3072
	ds_read_b128 v[18:21], v203
	ds_read_b128 v[22:25], v203 offset:1024
	ds_read_b128 v[154:157], v203 offset:2048
	ds_read_b128 v[158:161], v203 offset:3072
	s_add_u32 s22, s20, 0xfffc0080
	s_addc_u32 s23, s21, -1
	s_cmp_eq_u32 s63, 12
	s_cselect_b32 s25, s11, s23
	s_cselect_b32 s24, s49, s22
	s_cselect_b32 s23, s13, s62
	s_cselect_b32 s22, s60, s61
	v_lshl_add_u64 v[162:163], s[20:21], 0, v[180:181]
	s_add_i32 m0, s35, 0xc000
	ds_read_b128 v[206:209], v204
	ds_read_b128 v[210:213], v204 offset:1024
	ds_read_b128 v[214:217], v204 offset:2048
	ds_read_b128 v[218:221], v204 offset:3072
	ds_read_b128 v[222:225], v204 offset:4096
	ds_read_b128 v[226:229], v204 offset:5120
	ds_read_b128 v[230:233], v204 offset:6144
	ds_read_b128 v[234:237], v204 offset:7168
	global_load_lds_dwordx4 v[162:163], off
	v_lshl_add_u64 v[162:163], s[20:21], 0, v[182:183]
	s_add_i32 m0, s35, 0xe000
	s_nop 0
	global_load_lds_dwordx4 v[162:163], off
	s_waitcnt vmcnt(8)
	s_waitcnt lgkmcnt(0)
	s_barrier
	s_setprio 1
	s_waitcnt lgkmcnt(0)
	v_mfma_scale_f32_16x16x128_f8f6f4 v[150:153], v[2:7], v[206:211], v[150:153], v8, v212 op_sel_hi:[0,0,0] cbsz:2 blgp:2
	v_mfma_scale_f32_16x16x128_f8f6f4 v[138:141], v[10:15], v[206:211], v[138:141], v16, v212 op_sel_hi:[0,0,0] cbsz:2 blgp:2
	v_mfma_scale_f32_16x16x128_f8f6f4 v[134:137], v[2:7], v[214:219], v[134:137], v8, v220 op_sel_hi:[0,0,0] cbsz:2 blgp:2
	v_mfma_scale_f32_16x16x128_f8f6f4 v[122:125], v[10:15], v[214:219], v[122:125], v16, v220 op_sel_hi:[0,0,0] cbsz:2 blgp:2
	v_mfma_scale_f32_16x16x128_f8f6f4 v[118:121], v[2:7], v[222:227], v[118:121], v8, v228 op_sel_hi:[0,0,0] cbsz:2 blgp:2
	v_mfma_scale_f32_16x16x128_f8f6f4 v[106:109], v[10:15], v[222:227], v[106:109], v16, v228 op_sel_hi:[0,0,0] cbsz:2 blgp:2
	v_mfma_scale_f32_16x16x128_f8f6f4 v[102:105], v[2:7], v[230:235], v[102:105], v8, v236 op_sel_hi:[0,0,0] cbsz:2 blgp:2
	v_mfma_scale_f32_16x16x128_f8f6f4 v[90:93], v[10:15], v[230:235], v[90:93], v16, v236 op_sel_hi:[0,0,0] cbsz:2 blgp:2
	s_setprio 0
	s_setprio 1
	v_mfma_scale_f32_16x16x128_f8f6f4 v[146:149], v[18:23], v[206:211], v[146:149], v24, v212 op_sel_hi:[0,0,0] cbsz:2 blgp:2
	v_mfma_scale_f32_16x16x128_f8f6f4 v[142:145], v[154:159], v[206:211], v[142:145], v160, v212 op_sel_hi:[0,0,0] cbsz:2 blgp:2
	v_mfma_scale_f32_16x16x128_f8f6f4 v[130:133], v[18:23], v[214:219], v[130:133], v24, v220 op_sel_hi:[0,0,0] cbsz:2 blgp:2
	v_mfma_scale_f32_16x16x128_f8f6f4 v[126:129], v[154:159], v[214:219], v[126:129], v160, v220 op_sel_hi:[0,0,0] cbsz:2 blgp:2
	v_mfma_scale_f32_16x16x128_f8f6f4 v[114:117], v[18:23], v[222:227], v[114:117], v24, v228 op_sel_hi:[0,0,0] cbsz:2 blgp:2
	v_mfma_scale_f32_16x16x128_f8f6f4 v[110:113], v[154:159], v[222:227], v[110:113], v160, v228 op_sel_hi:[0,0,0] cbsz:2 blgp:2
	v_mfma_scale_f32_16x16x128_f8f6f4 v[98:101], v[18:23], v[230:235], v[98:101], v24, v236 op_sel_hi:[0,0,0] cbsz:2 blgp:2
	v_mfma_scale_f32_16x16x128_f8f6f4 v[94:97], v[154:159], v[230:235], v[94:97], v160, v236 op_sel_hi:[0,0,0] cbsz:2 blgp:2
	s_setprio 0
	s_barrier
	s_add_i32 s64, s42, s27
	v_lshl_add_u64 v[184:185], s[22:23], 0, v[172:173]
	s_mov_b32 m0, s64
	ds_read_b128 v[206:209], v204 offset:16384
	ds_read_b128 v[210:213], v204 offset:17408
	ds_read_b128 v[214:217], v204 offset:18432
	ds_read_b128 v[218:221], v204 offset:19456
	ds_read_b128 v[222:225], v204 offset:20480
	ds_read_b128 v[226:229], v204 offset:21504
	ds_read_b128 v[230:233], v204 offset:22528
	ds_read_b128 v[234:237], v204 offset:23552
	global_load_lds_dwordx4 v[184:185], off
	s_add_i32 m0, s64, 0x2000
	s_add_u32 s64, s22, 0x40000
	v_lshl_add_u64 v[186:187], s[22:23], 0, v[174:175]
	s_addc_u32 s65, s23, 0
	s_add_i32 s66, s43, s27
	global_load_lds_dwordx4 v[186:187], off
	v_lshl_add_u64 v[164:165], s[64:65], 0, v[172:173]
	s_mov_b32 m0, s66
	v_lshl_add_u64 v[188:189], s[24:25], 0, v[178:179]
	global_load_lds_dwordx4 v[164:165], off
	v_lshl_add_u64 v[164:165], s[64:65], 0, v[174:175]
	s_add_i32 m0, s66, 0x2000
	v_lshl_add_u64 v[190:191], s[24:25], 0, v[176:177]
	global_load_lds_dwordx4 v[164:165], off
	s_mov_b32 m0, s35
	s_nop 0
	global_load_lds_dwordx4 v[188:189], off
	s_mov_b32 m0, s36
	s_nop 0
	global_load_lds_dwordx4 v[190:191], off
	s_waitcnt vmcnt(8)
	s_waitcnt lgkmcnt(0)
	s_barrier
	s_setprio 1
	s_waitcnt lgkmcnt(0)
	v_mfma_scale_f32_16x16x128_f8f6f4 v[86:89], v[2:7], v[206:211], v[86:89], v8, v212 op_sel_hi:[0,0,0] cbsz:2 blgp:2
	v_mfma_scale_f32_16x16x128_f8f6f4 v[74:77], v[10:15], v[206:211], v[74:77], v16, v212 op_sel_hi:[0,0,0] cbsz:2 blgp:2
	v_mfma_scale_f32_16x16x128_f8f6f4 v[70:73], v[2:7], v[214:219], v[70:73], v8, v220 op_sel_hi:[0,0,0] cbsz:2 blgp:2
	v_mfma_scale_f32_16x16x128_f8f6f4 v[58:61], v[10:15], v[214:219], v[58:61], v16, v220 op_sel_hi:[0,0,0] cbsz:2 blgp:2
	v_mfma_scale_f32_16x16x128_f8f6f4 v[54:57], v[2:7], v[222:227], v[54:57], v8, v228 op_sel_hi:[0,0,0] cbsz:2 blgp:2
	v_mfma_scale_f32_16x16x128_f8f6f4 v[42:45], v[10:15], v[222:227], v[42:45], v16, v228 op_sel_hi:[0,0,0] cbsz:2 blgp:2
	v_mfma_scale_f32_16x16x128_f8f6f4 v[38:41], v[2:7], v[230:235], v[38:41], v8, v236 op_sel_hi:[0,0,0] cbsz:2 blgp:2
	v_mfma_scale_f32_16x16x128_f8f6f4 v[26:29], v[10:15], v[230:235], v[26:29], v16, v236 op_sel_hi:[0,0,0] cbsz:2 blgp:2
	s_setprio 0
	s_setprio 1
	v_mfma_scale_f32_16x16x128_f8f6f4 v[82:85], v[18:23], v[206:211], v[82:85], v24, v212 op_sel_hi:[0,0,0] cbsz:2 blgp:2
	v_mfma_scale_f32_16x16x128_f8f6f4 v[78:81], v[154:159], v[206:211], v[78:81], v160, v212 op_sel_hi:[0,0,0] cbsz:2 blgp:2
	v_mfma_scale_f32_16x16x128_f8f6f4 v[66:69], v[18:23], v[214:219], v[66:69], v24, v220 op_sel_hi:[0,0,0] cbsz:2 blgp:2
	v_mfma_scale_f32_16x16x128_f8f6f4 v[62:65], v[154:159], v[214:219], v[62:65], v160, v220 op_sel_hi:[0,0,0] cbsz:2 blgp:2
	v_mfma_scale_f32_16x16x128_f8f6f4 v[50:53], v[18:23], v[222:227], v[50:53], v24, v228 op_sel_hi:[0,0,0] cbsz:2 blgp:2
	v_mfma_scale_f32_16x16x128_f8f6f4 v[46:49], v[154:159], v[222:227], v[46:49], v160, v228 op_sel_hi:[0,0,0] cbsz:2 blgp:2
	v_mfma_scale_f32_16x16x128_f8f6f4 v[34:37], v[18:23], v[230:235], v[34:37], v24, v236 op_sel_hi:[0,0,0] cbsz:2 blgp:2
	v_mfma_scale_f32_16x16x128_f8f6f4 v[30:33], v[154:159], v[230:235], v[30:33], v160, v236 op_sel_hi:[0,0,0] cbsz:2 blgp:2
	s_setprio 0
	s_barrier
	s_add_i32 s64, 0, 0x18000
	s_add_i32 s65, 0, 0x1c000
	v_add_u32_e32 v166, s64, v198
	v_add_u32_e32 v167, s65, v198
	ds_read_b128 v[2:5], v166
	ds_read_b128 v[6:9], v166 offset:1024
	ds_read_b128 v[10:13], v166 offset:2048
	ds_read_b128 v[14:17], v166 offset:3072
	ds_read_b128 v[18:21], v167
	ds_read_b128 v[22:25], v167 offset:1024
	ds_read_b128 v[154:157], v167 offset:2048
	ds_read_b128 v[158:161], v167 offset:3072
	s_add_u32 s24, s24, 0x40000
	s_addc_u32 s25, s25, 0
	s_mov_b32 m0, s37
	v_lshl_add_u64 v[162:163], s[24:25], 0, v[178:179]
	ds_read_b128 v[206:209], v204 offset:32768
	ds_read_b128 v[210:213], v204 offset:33792
	ds_read_b128 v[214:217], v204 offset:34816
	ds_read_b128 v[218:221], v204 offset:35840
	ds_read_b128 v[222:225], v204 offset:36864
	ds_read_b128 v[226:229], v204 offset:37888
	ds_read_b128 v[230:233], v204 offset:38912
	ds_read_b128 v[234:237], v204 offset:39936
	global_load_lds_dwordx4 v[162:163], off
	v_lshl_add_u64 v[162:163], s[24:25], 0, v[176:177]
	s_mov_b32 m0, s38
	s_nop 0
	global_load_lds_dwordx4 v[162:163], off
	s_waitcnt vmcnt(8)
	s_waitcnt lgkmcnt(0)
	s_barrier
	s_setprio 1
	s_waitcnt lgkmcnt(0)
	v_mfma_scale_f32_16x16x128_f8f6f4 v[150:153], v[2:7], v[206:211], v[150:153], v8, v212 op_sel_hi:[0,0,0] cbsz:2 blgp:2
	v_mfma_scale_f32_16x16x128_f8f6f4 v[138:141], v[10:15], v[206:211], v[138:141], v16, v212 op_sel_hi:[0,0,0] cbsz:2 blgp:2
	v_mfma_scale_f32_16x16x128_f8f6f4 v[134:137], v[2:7], v[214:219], v[134:137], v8, v220 op_sel_hi:[0,0,0] cbsz:2 blgp:2
	v_mfma_scale_f32_16x16x128_f8f6f4 v[122:125], v[10:15], v[214:219], v[122:125], v16, v220 op_sel_hi:[0,0,0] cbsz:2 blgp:2
	v_mfma_scale_f32_16x16x128_f8f6f4 v[118:121], v[2:7], v[222:227], v[118:121], v8, v228 op_sel_hi:[0,0,0] cbsz:2 blgp:2
	v_mfma_scale_f32_16x16x128_f8f6f4 v[106:109], v[10:15], v[222:227], v[106:109], v16, v228 op_sel_hi:[0,0,0] cbsz:2 blgp:2
	v_mfma_scale_f32_16x16x128_f8f6f4 v[102:105], v[2:7], v[230:235], v[102:105], v8, v236 op_sel_hi:[0,0,0] cbsz:2 blgp:2
	v_mfma_scale_f32_16x16x128_f8f6f4 v[90:93], v[10:15], v[230:235], v[90:93], v16, v236 op_sel_hi:[0,0,0] cbsz:2 blgp:2
	s_setprio 0
	s_setprio 1
	v_mfma_scale_f32_16x16x128_f8f6f4 v[146:149], v[18:23], v[206:211], v[146:149], v24, v212 op_sel_hi:[0,0,0] cbsz:2 blgp:2
	v_mfma_scale_f32_16x16x128_f8f6f4 v[142:145], v[154:159], v[206:211], v[142:145], v160, v212 op_sel_hi:[0,0,0] cbsz:2 blgp:2
	v_mfma_scale_f32_16x16x128_f8f6f4 v[130:133], v[18:23], v[214:219], v[130:133], v24, v220 op_sel_hi:[0,0,0] cbsz:2 blgp:2
	v_mfma_scale_f32_16x16x128_f8f6f4 v[126:129], v[154:159], v[214:219], v[126:129], v160, v220 op_sel_hi:[0,0,0] cbsz:2 blgp:2
	v_mfma_scale_f32_16x16x128_f8f6f4 v[114:117], v[18:23], v[222:227], v[114:117], v24, v228 op_sel_hi:[0,0,0] cbsz:2 blgp:2
	v_mfma_scale_f32_16x16x128_f8f6f4 v[110:113], v[154:159], v[222:227], v[110:113], v160, v228 op_sel_hi:[0,0,0] cbsz:2 blgp:2
	v_mfma_scale_f32_16x16x128_f8f6f4 v[98:101], v[18:23], v[230:235], v[98:101], v24, v236 op_sel_hi:[0,0,0] cbsz:2 blgp:2
	v_mfma_scale_f32_16x16x128_f8f6f4 v[94:97], v[154:159], v[230:235], v[94:97], v160, v236 op_sel_hi:[0,0,0] cbsz:2 blgp:2
	s_setprio 0
	s_barrier
	s_add_i32 s24, s64, s27
	v_lshl_add_u64 v[164:165], v[184:185], 0, s[6:7]
	s_mov_b32 m0, s24
	ds_read_b128 v[206:209], v204 offset:49152
	ds_read_b128 v[210:213], v204 offset:50176
	ds_read_b128 v[214:217], v204 offset:51200
	ds_read_b128 v[218:221], v204 offset:52224
	ds_read_b128 v[222:225], v204 offset:53248
	ds_read_b128 v[226:229], v204 offset:54272
	ds_read_b128 v[230:233], v204 offset:55296
	ds_read_b128 v[234:237], v204 offset:56320
	global_load_lds_dwordx4 v[164:165], off
	s_add_i32 m0, s24, 0x2000
	s_add_u32 s22, s22, 0x40080
	v_lshl_add_u64 v[164:165], v[186:187], 0, s[6:7]
	s_addc_u32 s23, s23, 0
	s_add_i32 s24, s65, s27
	global_load_lds_dwordx4 v[164:165], off
	v_lshl_add_u64 v[164:165], s[22:23], 0, v[172:173]
	s_mov_b32 m0, s24
	s_nop 0
	global_load_lds_dwordx4 v[164:165], off
	v_lshl_add_u64 v[164:165], s[22:23], 0, v[174:175]
	s_add_i32 m0, s24, 0x2000
	s_nop 0
	global_load_lds_dwordx4 v[164:165], off
	v_lshl_add_u64 v[164:165], v[188:189], 0, s[6:7]
	s_mov_b32 m0, s39
	s_nop 0
	global_load_lds_dwordx4 v[164:165], off
	v_lshl_add_u64 v[164:165], v[190:191], 0, s[6:7]
	s_mov_b32 m0, s40
	s_nop 0
	global_load_lds_dwordx4 v[164:165], off
	s_waitcnt vmcnt(8)
	s_waitcnt lgkmcnt(0)
	s_barrier
	s_setprio 1
	s_waitcnt lgkmcnt(0)
	v_mfma_scale_f32_16x16x128_f8f6f4 v[86:89], v[2:7], v[206:211], v[86:89], v8, v212 op_sel_hi:[0,0,0] cbsz:2 blgp:2
	v_mfma_scale_f32_16x16x128_f8f6f4 v[74:77], v[10:15], v[206:211], v[74:77], v16, v212 op_sel_hi:[0,0,0] cbsz:2 blgp:2
	v_mfma_scale_f32_16x16x128_f8f6f4 v[70:73], v[2:7], v[214:219], v[70:73], v8, v220 op_sel_hi:[0,0,0] cbsz:2 blgp:2
	v_mfma_scale_f32_16x16x128_f8f6f4 v[58:61], v[10:15], v[214:219], v[58:61], v16, v220 op_sel_hi:[0,0,0] cbsz:2 blgp:2
	v_mfma_scale_f32_16x16x128_f8f6f4 v[54:57], v[2:7], v[222:227], v[54:57], v8, v228 op_sel_hi:[0,0,0] cbsz:2 blgp:2
	v_mfma_scale_f32_16x16x128_f8f6f4 v[42:45], v[10:15], v[222:227], v[42:45], v16, v228 op_sel_hi:[0,0,0] cbsz:2 blgp:2
	v_mfma_scale_f32_16x16x128_f8f6f4 v[38:41], v[2:7], v[230:235], v[38:41], v8, v236 op_sel_hi:[0,0,0] cbsz:2 blgp:2
	v_mfma_scale_f32_16x16x128_f8f6f4 v[26:29], v[10:15], v[230:235], v[26:29], v16, v236 op_sel_hi:[0,0,0] cbsz:2 blgp:2
	s_setprio 0
	s_setprio 1
	v_mfma_scale_f32_16x16x128_f8f6f4 v[82:85], v[18:23], v[206:211], v[82:85], v24, v212 op_sel_hi:[0,0,0] cbsz:2 blgp:2
	v_mfma_scale_f32_16x16x128_f8f6f4 v[78:81], v[154:159], v[206:211], v[78:81], v160, v212 op_sel_hi:[0,0,0] cbsz:2 blgp:2
	v_mfma_scale_f32_16x16x128_f8f6f4 v[66:69], v[18:23], v[214:219], v[66:69], v24, v220 op_sel_hi:[0,0,0] cbsz:2 blgp:2
	v_mfma_scale_f32_16x16x128_f8f6f4 v[62:65], v[154:159], v[214:219], v[62:65], v160, v220 op_sel_hi:[0,0,0] cbsz:2 blgp:2
	v_mfma_scale_f32_16x16x128_f8f6f4 v[50:53], v[18:23], v[222:227], v[50:53], v24, v228 op_sel_hi:[0,0,0] cbsz:2 blgp:2
	v_mfma_scale_f32_16x16x128_f8f6f4 v[46:49], v[154:159], v[222:227], v[46:49], v160, v228 op_sel_hi:[0,0,0] cbsz:2 blgp:2
	v_mfma_scale_f32_16x16x128_f8f6f4 v[34:37], v[18:23], v[230:235], v[34:37], v24, v236 op_sel_hi:[0,0,0] cbsz:2 blgp:2
	v_mfma_scale_f32_16x16x128_f8f6f4 v[30:33], v[154:159], v[230:235], v[30:33], v160, v236 op_sel_hi:[0,0,0] cbsz:2 blgp:2
	s_setprio 0
	s_barrier
	s_add_i32 s63, s63, 2
	s_add_u32 s20, s20, 0x100
	s_addc_u32 s21, s21, 0
	s_add_u32 s61, s61, 0x100
	s_addc_u32 s62, s62, 0
	s_cmp_gt_u32 s63, 13
	s_cbranch_scc0 .LBB0_1257
	s_and_b64 vcc, exec, s[8:9]
	s_cbranch_vccz .LBB0_1260
	s_barrier

.LBB0_1279:
	ds_read_b128 v[2:5], v195
	ds_read_b128 v[6:9], v195 offset:1024
	ds_read_b128 v[10:13], v195 offset:2048
	ds_read_b128 v[14:17], v195 offset:3072
	ds_read_b128 v[18:21], v196
	ds_read_b128 v[22:25], v196 offset:1024
	ds_read_b128 v[154:157], v196 offset:2048
	ds_read_b128 v[158:161], v196 offset:3072
	s_add_u32 s24, s22, 0xfffc0080
	s_addc_u32 s25, s23, -1
	s_cmp_eq_u32 s61, 12
	s_cselect_b32 s27, s11, s25
	s_cselect_b32 s26, s49, s24
	s_cselect_b32 s25, s13, s60
	s_cselect_b32 s24, s50, s51
	s_mov_b32 m0, s46
	v_lshl_add_u64 v[162:163], s[22:23], 0, v[180:181]
	ds_read_b128 v[206:209], v198
	ds_read_b128 v[210:213], v198 offset:1024
	ds_read_b128 v[214:217], v198 offset:2048
	ds_read_b128 v[218:221], v198 offset:3072
	ds_read_b128 v[222:225], v198 offset:4096
	ds_read_b128 v[226:229], v198 offset:5120
	ds_read_b128 v[230:233], v198 offset:6144
	ds_read_b128 v[234:237], v198 offset:7168
	global_load_lds_dwordx4 v[162:163], off
	v_lshl_add_u64 v[162:163], s[22:23], 0, v[182:183]
	s_add_i32 m0, s21, 0xe000
	s_nop 0
	global_load_lds_dwordx4 v[162:163], off
	s_waitcnt vmcnt(8)
	s_waitcnt lgkmcnt(0)
	s_barrier
	s_setprio 1
	s_waitcnt lgkmcnt(0)
	v_mfma_scale_f32_16x16x128_f8f6f4 v[150:153], v[2:7], v[206:211], v[150:153], v8, v212 op_sel_hi:[0,0,0] cbsz:2 blgp:2
	v_mfma_scale_f32_16x16x128_f8f6f4 v[138:141], v[10:15], v[206:211], v[138:141], v16, v212 op_sel_hi:[0,0,0] cbsz:2 blgp:2
	v_mfma_scale_f32_16x16x128_f8f6f4 v[134:137], v[2:7], v[214:219], v[134:137], v8, v220 op_sel_hi:[0,0,0] cbsz:2 blgp:2
	v_mfma_scale_f32_16x16x128_f8f6f4 v[122:125], v[10:15], v[214:219], v[122:125], v16, v220 op_sel_hi:[0,0,0] cbsz:2 blgp:2
	v_mfma_scale_f32_16x16x128_f8f6f4 v[118:121], v[2:7], v[222:227], v[118:121], v8, v228 op_sel_hi:[0,0,0] cbsz:2 blgp:2
	v_mfma_scale_f32_16x16x128_f8f6f4 v[106:109], v[10:15], v[222:227], v[106:109], v16, v228 op_sel_hi:[0,0,0] cbsz:2 blgp:2
	v_mfma_scale_f32_16x16x128_f8f6f4 v[102:105], v[2:7], v[230:235], v[102:105], v8, v236 op_sel_hi:[0,0,0] cbsz:2 blgp:2
	v_mfma_scale_f32_16x16x128_f8f6f4 v[90:93], v[10:15], v[230:235], v[90:93], v16, v236 op_sel_hi:[0,0,0] cbsz:2 blgp:2
	s_setprio 0
	s_setprio 1
	v_mfma_scale_f32_16x16x128_f8f6f4 v[146:149], v[18:23], v[206:211], v[146:149], v24, v212 op_sel_hi:[0,0,0] cbsz:2 blgp:2
	v_mfma_scale_f32_16x16x128_f8f6f4 v[142:145], v[154:159], v[206:211], v[142:145], v160, v212 op_sel_hi:[0,0,0] cbsz:2 blgp:2
	v_mfma_scale_f32_16x16x128_f8f6f4 v[130:133], v[18:23], v[214:219], v[130:133], v24, v220 op_sel_hi:[0,0,0] cbsz:2 blgp:2
	v_mfma_scale_f32_16x16x128_f8f6f4 v[126:129], v[154:159], v[214:219], v[126:129], v160, v220 op_sel_hi:[0,0,0] cbsz:2 blgp:2
	v_mfma_scale_f32_16x16x128_f8f6f4 v[114:117], v[18:23], v[222:227], v[114:117], v24, v228 op_sel_hi:[0,0,0] cbsz:2 blgp:2
	v_mfma_scale_f32_16x16x128_f8f6f4 v[110:113], v[154:159], v[222:227], v[110:113], v160, v228 op_sel_hi:[0,0,0] cbsz:2 blgp:2
	v_mfma_scale_f32_16x16x128_f8f6f4 v[98:101], v[18:23], v[230:235], v[98:101], v24, v236 op_sel_hi:[0,0,0] cbsz:2 blgp:2
	v_mfma_scale_f32_16x16x128_f8f6f4 v[94:97], v[154:159], v[230:235], v[94:97], v160, v236 op_sel_hi:[0,0,0] cbsz:2 blgp:2
	s_setprio 0
	s_barrier
	s_add_i32 s62, s42, s35
	v_lshl_add_u64 v[184:185], s[24:25], 0, v[176:177]
	s_mov_b32 m0, s62
	ds_read_b128 v[206:209], v198 offset:16384
	ds_read_b128 v[210:213], v198 offset:17408
	ds_read_b128 v[214:217], v198 offset:18432
	ds_read_b128 v[218:221], v198 offset:19456
	ds_read_b128 v[222:225], v198 offset:20480
	ds_read_b128 v[226:229], v198 offset:21504
	ds_read_b128 v[230:233], v198 offset:22528
	ds_read_b128 v[234:237], v198 offset:23552
	global_load_lds_dwordx4 v[184:185], off
	s_add_i32 m0, s62, 0x2000
	s_add_u32 s62, s24, 0x40000
	v_lshl_add_u64 v[186:187], s[24:25], 0, v[172:173]
	s_addc_u32 s63, s25, 0
	s_add_i32 s64, s43, s35
	global_load_lds_dwordx4 v[186:187], off
	v_lshl_add_u64 v[164:165], s[62:63], 0, v[176:177]
	s_mov_b32 m0, s64
	v_lshl_add_u64 v[188:189], s[26:27], 0, v[178:179]
	global_load_lds_dwordx4 v[164:165], off
	v_lshl_add_u64 v[164:165], s[62:63], 0, v[172:173]
	s_add_i32 m0, s64, 0x2000
	v_lshl_add_u64 v[190:191], s[26:27], 0, v[174:175]
	global_load_lds_dwordx4 v[164:165], off
	s_mov_b32 m0, s21
	s_nop 0
	global_load_lds_dwordx4 v[188:189], off
	s_mov_b32 m0, s36
	s_nop 0
	global_load_lds_dwordx4 v[190:191], off
	s_waitcnt vmcnt(8)
	s_waitcnt lgkmcnt(0)
	s_barrier
	s_setprio 1
	s_waitcnt lgkmcnt(0)
	v_mfma_scale_f32_16x16x128_f8f6f4 v[86:89], v[2:7], v[206:211], v[86:89], v8, v212 op_sel_hi:[0,0,0] cbsz:2 blgp:2
	v_mfma_scale_f32_16x16x128_f8f6f4 v[74:77], v[10:15], v[206:211], v[74:77], v16, v212 op_sel_hi:[0,0,0] cbsz:2 blgp:2
	v_mfma_scale_f32_16x16x128_f8f6f4 v[70:73], v[2:7], v[214:219], v[70:73], v8, v220 op_sel_hi:[0,0,0] cbsz:2 blgp:2
	v_mfma_scale_f32_16x16x128_f8f6f4 v[58:61], v[10:15], v[214:219], v[58:61], v16, v220 op_sel_hi:[0,0,0] cbsz:2 blgp:2
	v_mfma_scale_f32_16x16x128_f8f6f4 v[54:57], v[2:7], v[222:227], v[54:57], v8, v228 op_sel_hi:[0,0,0] cbsz:2 blgp:2
	v_mfma_scale_f32_16x16x128_f8f6f4 v[42:45], v[10:15], v[222:227], v[42:45], v16, v228 op_sel_hi:[0,0,0] cbsz:2 blgp:2
	v_mfma_scale_f32_16x16x128_f8f6f4 v[38:41], v[2:7], v[230:235], v[38:41], v8, v236 op_sel_hi:[0,0,0] cbsz:2 blgp:2
	v_mfma_scale_f32_16x16x128_f8f6f4 v[26:29], v[10:15], v[230:235], v[26:29], v16, v236 op_sel_hi:[0,0,0] cbsz:2 blgp:2
	s_setprio 0
	s_setprio 1
	v_mfma_scale_f32_16x16x128_f8f6f4 v[82:85], v[18:23], v[206:211], v[82:85], v24, v212 op_sel_hi:[0,0,0] cbsz:2 blgp:2
	v_mfma_scale_f32_16x16x128_f8f6f4 v[78:81], v[154:159], v[206:211], v[78:81], v160, v212 op_sel_hi:[0,0,0] cbsz:2 blgp:2
	v_mfma_scale_f32_16x16x128_f8f6f4 v[66:69], v[18:23], v[214:219], v[66:69], v24, v220 op_sel_hi:[0,0,0] cbsz:2 blgp:2
	v_mfma_scale_f32_16x16x128_f8f6f4 v[62:65], v[154:159], v[214:219], v[62:65], v160, v220 op_sel_hi:[0,0,0] cbsz:2 blgp:2
	v_mfma_scale_f32_16x16x128_f8f6f4 v[50:53], v[18:23], v[222:227], v[50:53], v24, v228 op_sel_hi:[0,0,0] cbsz:2 blgp:2
	v_mfma_scale_f32_16x16x128_f8f6f4 v[46:49], v[154:159], v[222:227], v[46:49], v160, v228 op_sel_hi:[0,0,0] cbsz:2 blgp:2
	v_mfma_scale_f32_16x16x128_f8f6f4 v[34:37], v[18:23], v[230:235], v[34:37], v24, v236 op_sel_hi:[0,0,0] cbsz:2 blgp:2
	v_mfma_scale_f32_16x16x128_f8f6f4 v[30:33], v[154:159], v[230:235], v[30:33], v160, v236 op_sel_hi:[0,0,0] cbsz:2 blgp:2
	s_setprio 0
	s_barrier
	s_add_i32 s62, 0, 0x18000
	s_add_i32 s63, 0, 0x1c000
	v_add_u32_e32 v2, s62, v194
	v_add_u32_e32 v6, s63, v194
	ds_read_b128 v[2:5], v166
	ds_read_b128 v[6:9], v166 offset:1024
	ds_read_b128 v[10:13], v166 offset:2048
	ds_read_b128 v[14:17], v166 offset:3072
	ds_read_b128 v[18:21], v167
	ds_read_b128 v[22:25], v167 offset:1024
	ds_read_b128 v[154:157], v167 offset:2048
	ds_read_b128 v[158:161], v167 offset:3072
	s_add_u32 s26, s26, 0x40000
	s_addc_u32 s27, s27, 0
	s_mov_b32 m0, s37
	v_lshl_add_u64 v[162:163], s[26:27], 0, v[178:179]
	ds_read_b128 v[206:209], v198 offset:32768
	ds_read_b128 v[210:213], v198 offset:33792
	ds_read_b128 v[214:217], v198 offset:34816
	ds_read_b128 v[218:221], v198 offset:35840
	ds_read_b128 v[222:225], v198 offset:36864
	ds_read_b128 v[226:229], v198 offset:37888
	ds_read_b128 v[230:233], v198 offset:38912
	ds_read_b128 v[234:237], v198 offset:39936
	global_load_lds_dwordx4 v[162:163], off
	v_lshl_add_u64 v[162:163], s[26:27], 0, v[174:175]
	s_mov_b32 m0, s38
	s_nop 0
	global_load_lds_dwordx4 v[162:163], off
	s_waitcnt vmcnt(8)
	s_waitcnt lgkmcnt(0)
	s_barrier
	s_setprio 1
	s_waitcnt lgkmcnt(0)
	v_mfma_scale_f32_16x16x128_f8f6f4 v[150:153], v[2:7], v[206:211], v[150:153], v8, v212 op_sel_hi:[0,0,0] cbsz:2 blgp:2
	v_mfma_scale_f32_16x16x128_f8f6f4 v[138:141], v[10:15], v[206:211], v[138:141], v16, v212 op_sel_hi:[0,0,0] cbsz:2 blgp:2
	v_mfma_scale_f32_16x16x128_f8f6f4 v[134:137], v[2:7], v[214:219], v[134:137], v8, v220 op_sel_hi:[0,0,0] cbsz:2 blgp:2
	v_mfma_scale_f32_16x16x128_f8f6f4 v[122:125], v[10:15], v[214:219], v[122:125], v16, v220 op_sel_hi:[0,0,0] cbsz:2 blgp:2
	v_mfma_scale_f32_16x16x128_f8f6f4 v[118:121], v[2:7], v[222:227], v[118:121], v8, v228 op_sel_hi:[0,0,0] cbsz:2 blgp:2
	v_mfma_scale_f32_16x16x128_f8f6f4 v[106:109], v[10:15], v[222:227], v[106:109], v16, v228 op_sel_hi:[0,0,0] cbsz:2 blgp:2
	v_mfma_scale_f32_16x16x128_f8f6f4 v[102:105], v[2:7], v[230:235], v[102:105], v8, v236 op_sel_hi:[0,0,0] cbsz:2 blgp:2
	v_mfma_scale_f32_16x16x128_f8f6f4 v[90:93], v[10:15], v[230:235], v[90:93], v16, v236 op_sel_hi:[0,0,0] cbsz:2 blgp:2
	s_setprio 0
	s_setprio 1
	v_mfma_scale_f32_16x16x128_f8f6f4 v[146:149], v[18:23], v[206:211], v[146:149], v24, v212 op_sel_hi:[0,0,0] cbsz:2 blgp:2
	v_mfma_scale_f32_16x16x128_f8f6f4 v[142:145], v[154:159], v[206:211], v[142:145], v160, v212 op_sel_hi:[0,0,0] cbsz:2 blgp:2
	v_mfma_scale_f32_16x16x128_f8f6f4 v[130:133], v[18:23], v[214:219], v[130:133], v24, v220 op_sel_hi:[0,0,0] cbsz:2 blgp:2
	v_mfma_scale_f32_16x16x128_f8f6f4 v[126:129], v[154:159], v[214:219], v[126:129], v160, v220 op_sel_hi:[0,0,0] cbsz:2 blgp:2
	v_mfma_scale_f32_16x16x128_f8f6f4 v[114:117], v[18:23], v[222:227], v[114:117], v24, v228 op_sel_hi:[0,0,0] cbsz:2 blgp:2
	v_mfma_scale_f32_16x16x128_f8f6f4 v[110:113], v[154:159], v[222:227], v[110:113], v160, v228 op_sel_hi:[0,0,0] cbsz:2 blgp:2
	v_mfma_scale_f32_16x16x128_f8f6f4 v[98:101], v[18:23], v[230:235], v[98:101], v24, v236 op_sel_hi:[0,0,0] cbsz:2 blgp:2
	v_mfma_scale_f32_16x16x128_f8f6f4 v[94:97], v[154:159], v[230:235], v[94:97], v160, v236 op_sel_hi:[0,0,0] cbsz:2 blgp:2
	s_setprio 0
	s_barrier
	s_add_i32 s26, s62, s35
	v_lshl_add_u64 v[164:165], v[184:185], 0, s[6:7]
	s_mov_b32 m0, s26
	ds_read_b128 v[206:209], v198 offset:49152
	ds_read_b128 v[210:213], v198 offset:50176
	ds_read_b128 v[214:217], v198 offset:51200
	ds_read_b128 v[218:221], v198 offset:52224
	ds_read_b128 v[222:225], v198 offset:53248
	ds_read_b128 v[226:229], v198 offset:54272
	ds_read_b128 v[230:233], v198 offset:55296
	ds_read_b128 v[234:237], v198 offset:56320
	global_load_lds_dwordx4 v[164:165], off
	s_add_i32 m0, s26, 0x2000
	s_add_u32 s24, s24, 0x40080
	v_lshl_add_u64 v[164:165], v[186:187], 0, s[6:7]
	s_addc_u32 s25, s25, 0
	s_add_i32 s26, s63, s35
	global_load_lds_dwordx4 v[164:165], off
	v_lshl_add_u64 v[164:165], s[24:25], 0, v[176:177]
	s_mov_b32 m0, s26
	s_nop 0
	global_load_lds_dwordx4 v[164:165], off
	v_lshl_add_u64 v[164:165], s[24:25], 0, v[172:173]
	s_add_i32 m0, s26, 0x2000
	s_nop 0
	global_load_lds_dwordx4 v[164:165], off
	v_lshl_add_u64 v[164:165], v[188:189], 0, s[6:7]
	s_mov_b32 m0, s40
	s_nop 0
	global_load_lds_dwordx4 v[164:165], off
	v_lshl_add_u64 v[164:165], v[190:191], 0, s[6:7]
	s_mov_b32 m0, s41
	s_nop 0
	global_load_lds_dwordx4 v[164:165], off
	s_waitcnt vmcnt(8)
	s_waitcnt lgkmcnt(0)
	s_barrier
	s_setprio 1
	s_waitcnt lgkmcnt(0)
	v_mfma_scale_f32_16x16x128_f8f6f4 v[86:89], v[2:7], v[206:211], v[86:89], v8, v212 op_sel_hi:[0,0,0] cbsz:2 blgp:2
	v_mfma_scale_f32_16x16x128_f8f6f4 v[74:77], v[10:15], v[206:211], v[74:77], v16, v212 op_sel_hi:[0,0,0] cbsz:2 blgp:2
	v_mfma_scale_f32_16x16x128_f8f6f4 v[70:73], v[2:7], v[214:219], v[70:73], v8, v220 op_sel_hi:[0,0,0] cbsz:2 blgp:2
	v_mfma_scale_f32_16x16x128_f8f6f4 v[58:61], v[10:15], v[214:219], v[58:61], v16, v220 op_sel_hi:[0,0,0] cbsz:2 blgp:2
	v_mfma_scale_f32_16x16x128_f8f6f4 v[54:57], v[2:7], v[222:227], v[54:57], v8, v228 op_sel_hi:[0,0,0] cbsz:2 blgp:2
	v_mfma_scale_f32_16x16x128_f8f6f4 v[42:45], v[10:15], v[222:227], v[42:45], v16, v228 op_sel_hi:[0,0,0] cbsz:2 blgp:2
	v_mfma_scale_f32_16x16x128_f8f6f4 v[38:41], v[2:7], v[230:235], v[38:41], v8, v236 op_sel_hi:[0,0,0] cbsz:2 blgp:2
	v_mfma_scale_f32_16x16x128_f8f6f4 v[26:29], v[10:15], v[230:235], v[26:29], v16, v236 op_sel_hi:[0,0,0] cbsz:2 blgp:2
	s_setprio 0
	s_setprio 1
	v_mfma_scale_f32_16x16x128_f8f6f4 v[82:85], v[18:23], v[206:211], v[82:85], v24, v212 op_sel_hi:[0,0,0] cbsz:2 blgp:2
	v_mfma_scale_f32_16x16x128_f8f6f4 v[78:81], v[154:159], v[206:211], v[78:81], v160, v212 op_sel_hi:[0,0,0] cbsz:2 blgp:2
	v_mfma_scale_f32_16x16x128_f8f6f4 v[66:69], v[18:23], v[214:219], v[66:69], v24, v220 op_sel_hi:[0,0,0] cbsz:2 blgp:2
	v_mfma_scale_f32_16x16x128_f8f6f4 v[62:65], v[154:159], v[214:219], v[62:65], v160, v220 op_sel_hi:[0,0,0] cbsz:2 blgp:2
	v_mfma_scale_f32_16x16x128_f8f6f4 v[50:53], v[18:23], v[222:227], v[50:53], v24, v228 op_sel_hi:[0,0,0] cbsz:2 blgp:2
	v_mfma_scale_f32_16x16x128_f8f6f4 v[46:49], v[154:159], v[222:227], v[46:49], v160, v228 op_sel_hi:[0,0,0] cbsz:2 blgp:2
	v_mfma_scale_f32_16x16x128_f8f6f4 v[34:37], v[18:23], v[230:235], v[34:37], v24, v236 op_sel_hi:[0,0,0] cbsz:2 blgp:2
	v_mfma_scale_f32_16x16x128_f8f6f4 v[30:33], v[154:159], v[230:235], v[30:33], v160, v236 op_sel_hi:[0,0,0] cbsz:2 blgp:2
	s_setprio 0
	s_barrier
	s_add_i32 s61, s61, 2
	s_add_u32 s22, s22, 0x100
	s_addc_u32 s23, s23, 0
	s_add_u32 s51, s51, 0x100
	s_addc_u32 s60, s60, 0
	s_cmp_gt_u32 s61, 13
	s_cbranch_scc0 .LBB0_1279
	s_and_b64 vcc, exec, s[8:9]
	s_cbranch_vccz .LBB0_1282
	s_barrier
